# barrier acquire-invalidate hoisted behind the arrival atomic (overlaps the wait)
# speedup vs baseline: 1.0131x; 1.0131x over previous
.LBB0_234:
	v_readlane_b32 s4, v253, 25
	s_lshl_b32 s4, s4, 8
	v_readlane_b32 s6, v253, 21
	v_readlane_b32 s7, v253, 22
	s_add_u32 s4, s6, s4
	s_addc_u32 s5, s7, 0
	v_mov_b32_e32 v1, 0x1000
	v_mov_b32_e32 v3, 1
	global_atomic_add v3, v1, v3, s[4:5] offset:1024 sc0
	buffer_inv sc1
	v_cvt_f32_u32_e32 v1, v2
	v_sub_u32_e32 v4, 0, v2
	s_add_u32 s4, s4, 0x2400
	s_addc_u32 s5, s5, 0
	v_rcp_iflag_f32_e32 v1, v1
	s_nop 0
	v_mul_f32_e32 v1, 0x4f7ffffe, v1
	v_cvt_u32_f32_e32 v1, v1
	v_mul_lo_u32 v4, v4, v1
	v_mul_hi_u32 v4, v1, v4
	v_add_u32_e32 v1, v1, v4
	s_waitcnt vmcnt(1)
	v_mul_hi_u32 v1, v3, v1
	v_mul_lo_u32 v4, v1, v2
	v_sub_u32_e32 v4, v3, v4
	v_add_u32_e32 v5, 1, v1
	v_cmp_ge_u32_e32 vcc, v4, v2
	v_add_u32_e32 v3, 1, v3
	s_nop 0
	v_cndmask_b32_e32 v1, v1, v5, vcc
	v_sub_u32_e32 v5, v4, v2
	v_cndmask_b32_e32 v4, v4, v5, vcc
	v_add_u32_e32 v5, 1, v1
	v_cmp_ge_u32_e32 vcc, v4, v2
	s_nop 1
	v_cndmask_b32_e32 v1, v1, v5, vcc
	v_mul_lo_u32 v4, v2, v1
	v_add_u32_e32 v2, v4, v2
	v_cmp_ne_u32_e32 vcc, v3, v2
	s_and_saveexec_b64 s[6:7], vcc
	s_xor_b64 s[6:7], exec, s[6:7]
	s_cbranch_execz .LBB0_248
	s_waitcnt lgkmcnt(0)
	v_mov_b32_e32 v0, 0
	global_load_dword v2, v0, s[4:5] sc1
	s_waitcnt vmcnt(0)
	v_cmp_eq_u32_e32 vcc, v2, v1
	s_and_saveexec_b64 s[8:9], vcc
	s_cbranch_execz .LBB0_247
	s_mov_b32 s20, 1
	s_mov_b64 s[10:11], 0
	s_branch .LBB0_238

.LBB0_247:
	s_or_b64 exec, exec, s[8:9]
	s_waitcnt vmcnt(0)
	s_waitcnt vmcnt(0)

.LBB0_265:
	s_or_b64 exec, exec, s[2:3]
	v_mov_b32_e32 v0, 0
	v_mov_b32_e32 v1, 1
	s_waitcnt vmcnt(0)
	global_atomic_add v0, v1, s[4:5]
	s_waitcnt vmcnt(0)

.LBB0_315:
	v_readlane_b32 s2, v253, 25
	s_lshl_b32 s2, s2, 8
	v_readlane_b32 s4, v253, 21
	v_readlane_b32 s5, v253, 22
	s_add_u32 s2, s4, s2
	s_addc_u32 s3, s5, 0
	v_mov_b32_e32 v1, 0x1000
	v_mov_b32_e32 v3, 1
	global_atomic_add v3, v1, v3, s[2:3] offset:1024 sc0
	buffer_inv sc1
	v_cvt_f32_u32_e32 v1, v2
	v_sub_u32_e32 v4, 0, v2
	v_rcp_iflag_f32_e32 v1, v1
	s_nop 0
	v_mul_f32_e32 v1, 0x4f7ffffe, v1
	v_cvt_u32_f32_e32 v1, v1
	v_mul_lo_u32 v4, v4, v1
	v_mul_hi_u32 v4, v1, v4
	v_add_u32_e32 v1, v1, v4
	s_waitcnt vmcnt(1)
	v_mul_hi_u32 v1, v3, v1
	v_mul_lo_u32 v4, v1, v2
	v_sub_u32_e32 v4, v3, v4
	v_add_u32_e32 v5, 1, v1
	v_cmp_ge_u32_e32 vcc, v4, v2
	v_add_u32_e32 v3, 1, v3
	s_nop 0
	v_cndmask_b32_e32 v1, v1, v5, vcc
	v_sub_u32_e32 v5, v4, v2
	v_cndmask_b32_e32 v4, v4, v5, vcc
	v_add_u32_e32 v5, 1, v1
	v_cmp_ge_u32_e32 vcc, v4, v2
	s_nop 1
	v_cndmask_b32_e32 v1, v1, v5, vcc
	v_mul_lo_u32 v4, v2, v1
	v_add_u32_e32 v2, v4, v2
	v_cmp_ne_u32_e32 vcc, v3, v2
	s_and_saveexec_b64 s[4:5], vcc
	s_xor_b64 s[4:5], exec, s[4:5]
	s_cbranch_execz .LBB0_329
	s_waitcnt lgkmcnt(0)
	v_mov_b32_e32 v0, 0x2000
	global_load_dword v0, v0, s[2:3] offset:1024 sc1
	s_add_u32 s10, s2, 0x2400
	s_addc_u32 s11, s3, 0
	s_waitcnt vmcnt(0)
	v_cmp_eq_u32_e32 vcc, v0, v1
	s_and_saveexec_b64 s[6:7], vcc
	s_cbranch_execz .LBB0_328
	s_add_u32 s8, s94, 0x4200
	s_addc_u32 s9, s95, 0
	s_mov_b32 s22, 1
	s_mov_b64 s[12:13], 0
	v_mov_b32_e32 v0, 0
	s_branch .LBB0_319

.LBB0_328:
	s_or_b64 exec, exec, s[6:7]
	s_waitcnt vmcnt(0)
	s_waitcnt vmcnt(0)

.LBB0_346:
	s_or_b64 exec, exec, s[4:5]
	v_mov_b32_e32 v0, 0x2000
	v_mov_b32_e32 v1, 1
	s_waitcnt vmcnt(0)
	global_atomic_add v0, v1, s[2:3] offset:1024
	s_waitcnt vmcnt(0)
